# phase 3 expert-weight conversion runs the four-deep phase-7 conversion loop (shared code, parametrised queue word / item range) instead of the two-deep copy
# speedup vs baseline: 1.0067x; 1.0043x over previous
.LBB0_893:
	v_readlane_b32 s3, v254, 44
	s_lshl_b32 s0, s3, 14
	s_lshl_b32 s2, s3, 3
	s_lshl_b32 s3, s3, 8
	s_and_b32 s4, s3, 0x700
	s_add_i32 s0, s0, 0
	s_lshl_b32 s5, s4, 10
	v_readlane_b32 s6, v254, 57
	v_readlane_b32 s7, v254, 58
	s_add_u32 s5, s6, s5
	v_lshrrev_b32_e32 v66, 3, v1
	s_waitcnt vmcnt(14)
	v_and_b32_e32 v2, 28, v167
	v_and_b32_e32 v76, 56, v179
	s_addc_u32 s20, s7, 0
	v_mov_b32_e32 v69, 0
	v_lshl_add_u32 v3, v2, 2, s0
	v_mul_u32_u24_e32 v4, 0x84, v66
	v_mul_u32_u24_e32 v5, 0x84, v76
	s_waitcnt vmcnt(4)
	v_lshlrev_b32_e32 v6, 2, v66
	s_add_i32 s21, 0, 0x26600
	v_readlane_b32 s76, v254, 49
	s_mov_b32 s1, 0
	v_or_b32_e32 v70, 8, v66
	v_or_b32_e32 v72, 16, v66
	v_or_b32_e32 v74, 24, v66
	v_or_b32_e32 v67, 32, v66
	v_or_b32_e32 v71, 40, v66
	v_or_b32_e32 v73, 48, v66
	v_or_b32_e32 v75, 56, v66
	v_mov_b32_e32 v77, v69
	v_add3_u32 v78, s0, v5, v6
	v_mov_b32_e32 v79, s21
	s_movk_i32 s22, 0x3ff
	s_lshl_b32 s23, s4, 2
	s_mov_b32 s4, 0x42000000
	v_lshlrev_b32_e32 v68, 2, v2
	v_add_u32_e32 v80, v3, v4
	v_readlane_b32 s77, v254, 50
	v_readlane_b32 s78, v254, 51
	v_readlane_b32 s79, v254, 52
	v_readlane_b32 s72, v255, 9
	v_readlane_b32 s81, v255, 8
	v_readlane_b32 s69, v254, 59
	v_readlane_b32 s73, v254, 55
	v_readlane_b32 s80, v254, 56
	v_lshlrev_b32_e32 v4, 2, v0
	s_mov_b32 s98, 1
	s_mov_b32 s99, 0
	s_movk_i32 s100, 0x3ff
	s_mov_b32 s101, 0
	s_branch mkcq_common
mkcq_p3ret:
	s_mov_b32 s98, 0

.LBB0_1286:
	s_mov_b32 s98, 0
	s_movk_i32 s99, 0x400
	s_movk_i32 s100, 0x5ff
	s_movk_i32 s101, 0x100
mkcq_common:
	v_readlane_b32 s2, v254, 44
	s_lshl_b32 s0, s2, 14
	s_lshl_b32 s3, s2, 3
	s_lshl_b32 s2, s2, 8
	s_and_b32 s2, s2, 0x700
	s_add_i32 s0, s0, 0
	s_lshl_b32 s4, s2, 10
	v_readlane_b32 s6, v254, 57
	v_readlane_b32 s7, v254, 58
	s_add_u32 s30, s6, s4
	v_lshrrev_b32_e32 v134, 3, v1
	v_and_b32_e32 v2, 28, v4
	v_and_b32_e32 v132, 56, v179
	s_addc_u32 s31, s7, 0
	v_mov_b32_e32 v131, 0
	v_lshl_add_u32 v3, v2, 2, s0
	v_mul_u32_u24_e32 v4, 0x84, v134
	v_mul_u32_u24_e32 v5, 0x84, v132
	v_lshlrev_b32_e32 v6, 2, v134
	s_add_i32 s33, 0, 0x26600
	s_mov_b32 s1, 0
	v_or_b32_e32 v135, 8, v134
	v_or_b32_e32 v136, 16, v134
	v_or_b32_e32 v137, 24, v134
	v_or_b32_e32 v138, 32, v134
	v_or_b32_e32 v139, 40, v134
	v_or_b32_e32 v140, 48, v134
	v_or_b32_e32 v141, 56, v134
	v_mov_b32_e32 v133, v131
	v_add3_u32 v142, s0, v5, v6
	v_mov_b32_e32 v143, s33
	s_mov_b32 s34, s100
	s_lshl_b32 s35, s2, 2
	s_mov_b32 s2, 0x42000000
	v_lshlrev_b32_e32 v130, 2, v2
	v_add_u32_e32 v144, v3, v4
	s_branch .LBB0_1290

.LBB0_1290:
	s_waitcnt vmcnt(0)
	s_barrier
	s_mov_b64 s[4:5], exec
	v_readlane_b32 s6, v254, 5
	v_readlane_b32 s7, v254, 6
	s_and_b64 s[6:7], s[4:5], s[6:7]
	s_mov_b64 exec, s[6:7]
	s_cbranch_execz .LBB0_1294
	s_mov_b64 s[8:9], exec
	v_mbcnt_lo_u32_b32 v2, s8, 0
	v_mbcnt_hi_u32_b32 v2, s9, v2
	v_cmp_eq_u32_e32 vcc, 0, v2
	s_and_saveexec_b64 s[6:7], vcc
	s_cbranch_execz .LBB0_1293
	s_bcnt1_i32_b64 s0, s[8:9]
	v_mov_b32_e32 v3, s0
	v_mov_b32_e32 v6, s101
	global_atomic_add v3, v6, v3, s[96:97] offset:768 sc0
.LBB0_1293:
	s_or_b64 exec, exec, s[6:7]
	s_waitcnt vmcnt(0)
	v_readfirstlane_b32 s0, v3
	v_mov_b32_e32 v3, s33
	s_nop 0
	v_add_u32_e32 v2, s0, v2
	v_add_u32_e32 v2, s99, v2
	ds_write_b32 v3, v2

.LBB0_1334:
	s_cmp_eq_u32 s98, 1
	s_cbranch_scc1 mkcq_p3ret
	v_readlane_b32 s48, v254, 53
	v_readlane_b32 s49, v254, 54
	s_cmp_lt_i32 s49, 9
	s_barrier
	s_cbranch_scc1 .LBB0_1388
	s_waitcnt vmcnt(0)
	s_barrier
	s_mov_b64 s[0:1], exec
	v_readlane_b32 s2, v254, 5
	v_readlane_b32 s3, v254, 6
	s_and_b64 s[2:3], s[0:1], s[2:3]
	s_mov_b64 exec, s[2:3]
	s_cbranch_execz .LBB0_1387
	s_add_i32 s2, 0, 0x26160
	v_mov_b32_e32 v2, s2
	s_waitcnt vmcnt(0) expcnt(0) lgkmcnt(0)
	ds_read_b32 v4, v2
	s_add_i32 s2, 0, 0x26164
	v_mov_b32_e32 v2, s2
	ds_read_b32 v2, v2
	s_waitcnt lgkmcnt(1)
	v_cmp_ne_u32_e32 vcc, 0, v4
	s_cbranch_vccnz .LBB0_1351
	v_readlane_b32 s2, v254, 0
	v_readlane_b32 s3, v254, 1
	s_load_dwordx2 s[6:7], s[2:3], 0x4
	s_add_u32 s2, s96, 0x4200
	s_addc_u32 s3, s97, 0
	s_add_u32 s4, s96, 0x4400
	s_addc_u32 s5, s97, 0
	s_waitcnt lgkmcnt(0)
	s_mul_i32 s33, s6, s72
	s_add_u32 s6, s96, 0x4500
	s_mul_i32 s33, s33, s7
	s_addc_u32 s7, s97, 0
	s_add_u32 s8, s96, 0x4600
	s_addc_u32 s9, s97, 0
	s_add_u32 s10, s96, 0x4700
	s_addc_u32 s11, s97, 0
	s_add_u32 s18, s96, 0x4800
	s_addc_u32 s19, s97, 0
	s_add_u32 s20, s96, 0x4900
	s_addc_u32 s21, s97, 0
	s_add_u32 s22, s96, 0x4a00
	s_addc_u32 s23, s97, 0
	s_add_u32 s24, s96, 0x4b00
	s_addc_u32 s25, s97, 0
	s_add_u32 s26, s96, 0x4c00
	s_addc_u32 s27, s97, 0
	s_add_u32 s28, s96, 0x4d00
	s_addc_u32 s29, s97, 0
	s_add_u32 s30, s96, 0x4e00
	s_addc_u32 s31, s97, 0
	s_add_u32 s34, s96, 0x4f00
	s_addc_u32 s35, s97, 0
	s_add_u32 s36, s96, 0x5000
	s_addc_u32 s37, s97, 0
	s_add_u32 s38, s96, 0x5100
	s_addc_u32 s39, s97, 0
	s_add_u32 s40, s96, 0x5200
	s_addc_u32 s41, s97, 0
	s_add_u32 s42, s96, 0x5300
	s_addc_u32 s43, s97, 0
	s_mov_b32 s50, 1
	v_mov_b32_e32 v18, 0
	s_branch .LBB0_1339

	.amdhsa_kernel _Z6mk_fwd4Args
		.amdhsa_group_segment_fixed_size 0
		.amdhsa_private_segment_fixed_size 0
		.amdhsa_kernarg_size 448
		.amdhsa_user_sgpr_count 2
		.amdhsa_user_sgpr_dispatch_ptr 0
		.amdhsa_user_sgpr_queue_ptr 0
		.amdhsa_user_sgpr_kernarg_segment_ptr 1
		.amdhsa_user_sgpr_dispatch_id 0
		.amdhsa_user_sgpr_kernarg_preload_length 0
		.amdhsa_user_sgpr_kernarg_preload_offset 0
		.amdhsa_user_sgpr_private_segment_size 0
		.amdhsa_uses_dynamic_stack 0
		.amdhsa_enable_private_segment 0
		.amdhsa_system_sgpr_workgroup_id_x 1
		.amdhsa_system_sgpr_workgroup_id_y 0
		.amdhsa_system_sgpr_workgroup_id_z 0
		.amdhsa_system_sgpr_workgroup_info 0
		.amdhsa_system_vgpr_workitem_id 0
		.amdhsa_next_free_vgpr 256
		.amdhsa_next_free_sgpr 102
		.amdhsa_accum_offset 256
		.amdhsa_reserve_vcc 1
		.amdhsa_float_round_mode_32 0
		.amdhsa_float_round_mode_16_64 0
		.amdhsa_float_denorm_mode_32 3
		.amdhsa_float_denorm_mode_16_64 3
		.amdhsa_dx10_clamp 1
		.amdhsa_ieee_mode 1
		.amdhsa_fp16_overflow 0
		.amdhsa_tg_split 0
		.amdhsa_exception_fp_ieee_invalid_op 0
		.amdhsa_exception_fp_denorm_src 0
		.amdhsa_exception_fp_ieee_div_zero 0
		.amdhsa_exception_fp_ieee_overflow 0
		.amdhsa_exception_fp_ieee_underflow 0
		.amdhsa_exception_fp_ieee_inexact 0
		.amdhsa_exception_int_div_zero 0
	.end_amdhsa_kernel

amdhsa.kernels:
  - .agpr_count:     0
    .args:
      - .offset:         0
        .size:           192
        .value_kind:     by_value
      - .offset:         192
        .size:           4
        .value_kind:     hidden_block_count_x
      - .offset:         196
        .size:           4
        .value_kind:     hidden_block_count_y
      - .offset:         200
        .size:           4
        .value_kind:     hidden_block_count_z
      - .offset:         204
        .size:           2
        .value_kind:     hidden_group_size_x
      - .offset:         206
        .size:           2
        .value_kind:     hidden_group_size_y
      - .offset:         208
        .size:           2
        .value_kind:     hidden_group_size_z
      - .offset:         210
        .size:           2
        .value_kind:     hidden_remainder_x
      - .offset:         212
        .size:           2
        .value_kind:     hidden_remainder_y
      - .offset:         214
        .size:           2
        .value_kind:     hidden_remainder_z
      - .offset:         232
        .size:           8
        .value_kind:     hidden_global_offset_x
      - .offset:         240
        .size:           8
        .value_kind:     hidden_global_offset_y
      - .offset:         248
        .size:           8
        .value_kind:     hidden_global_offset_z
      - .offset:         256
        .size:           2
        .value_kind:     hidden_grid_dims
      - .offset:         312
        .size:           4
        .value_kind:     hidden_dynamic_lds_size
    .group_segment_fixed_size: 0
    .kernarg_segment_align: 8
    .kernarg_segment_size: 448
    .language:       OpenCL C
    .language_version:
      - 2
      - 0
    .max_flat_workgroup_size: 512
    .name:           _Z6mk_fwd4Args
    .private_segment_fixed_size: 0
    .sgpr_count:     108
    .sgpr_spill_count: 95
    .symbol:         _Z6mk_fwd4Args.kd
    .uniform_work_group_size: 1
    .uses_dynamic_stack: false
    .vgpr_count:     256
    .vgpr_spill_count: 0
    .wavefront_size: 64
